# P9 K-loop: trailing wave group issues its B half-tile pieces one interval earlier, between the MFMAs of its preceding MFMA interval (with the leading group's later waits: one more interval of lead for
# baseline (speedup 1.0000x reference)
; #define PG8_STAGE(bufoff, gbase, voff) do { PG8_GLDS((const char*)(gbase), (voff)[0], ldsb + (bufoff)); PG8_GLDS((const char*)(gbase), (voff)[1], ldsb + (bufoff) + 8192u); } while (0)
; #define PG8_STAGEA(bufoff, gbase, o0, o1) do { PG8_GLDS((const char*)(gbase), (o0), ldsb + (bufoff)); PG8_GLDS((const char*)(gbase), (o1), ldsb + (bufoff) + 8192u); } while (0)
; #define PG8_LDA(dst, b, h) do { if constexpr (F8) { _Pragma("unroll") for (int m = 0; m < 4; ++m) dst##8[m] = PG8_LD32(lds + PG8_SA(b, h) + aoff + m * 2048); } else { \
;         _Pragma("unroll") for (int m = 0; m < 4; ++m) _Pragma("unroll") for (int k = 0; k < 2; ++k) dst[m][k] = *(const LAS bf16x8*)(lds + PG8_SA(b, h) + aoff + m * 2048 + k * 1024); } } while (0)
; #define PG8_WAIT_VX() do { if (relax) asm volatile("s_waitcnt vmcnt(%0)" :: "n"(8 + Epi::RELAX) : "memory"); else PG8_WAIT_V(8); } while (0)
; #define PG8_WAIT_L(n) asm volatile("s_waitcnt lgkmcnt(" #n ")" ::: "memory")
; #define PG8_BAR __builtin_amdgcn_s_barrier()
; #define PG8_SCHED __builtin_amdgcn_sched_barrier(0)
; template <class Epi, class Sched, bool F8 = false, bool PF = false, bool I8 = false, int PID = -1>
; __device__ __forceinline__ void gemm_phase(LAS unsigned char* lds, LAS unsigned char* xlds, const int RP, const int RPB, const int nt, const Sched& S, const Epi& E, const int stagger_ticks) {
;     ...
;             PG8_LDA(At, 0, 1); PG8_STAGE(PG8_SB(0, 0), b2, voffB); PG8_STAGE(PG8_SB(0, 1), b2 + hstepB, voffB); PG8_STAGEA(PG8_SA(0, 0), a2, vA0, vA1);
;             PG8_WAIT_VX(); PG8_WAIT_L(0); PG8_BAR; PG8_MMA(1, 0, At, B0); PG8_MMA(1, 1, At, B1); PG8_BAR; PG8_SCHED;
.LBB0_1062:
	s_add_u32 s30, s26, 0xfffe0080
	s_addc_u32 s31, s27, -1
	s_cmp_eq_u32 s73, 4
	s_cselect_b32 s38, s6, s30
	s_cselect_b32 s39, s7, s31
	s_cselect_b32 s34, s8, s25
	s_cselect_b32 s35, s9, s71
	s_add_u32 s30, s38, 0x80
	s_addc_u32 s31, s39, 0
	s_add_u32 s36, s34, 0x80
	s_addc_u32 s37, s35, 0
	ds_read_b128 v[170:173], v169 offset:16384
	ds_read_b128 v[174:177], v169 offset:17408
	ds_read_b128 v[178:181], v169 offset:18432
	ds_read_b128 v[182:185], v169 offset:19456
	ds_read_b128 v[186:189], v169 offset:20480
	ds_read_b128 v[190:193], v169 offset:21504
	ds_read_b128 v[194:197], v169 offset:22528
	ds_read_b128 v[198:201], v169 offset:23552
	s_and_b64 vcc, exec, s[18:19]
	s_cbranch_vccz .Lmy_g9s4
	s_add_i32 s75, s74, 0x10000
	s_mov_b32 m0, s75
	s_nop 0
	global_load_lds_dwordx4 v166, s[34:35]
	s_add_i32 s75, s74, 0x12000
	s_mov_b32 m0, s75
	s_nop 0
	global_load_lds_dwordx4 v167, s[34:35]
	s_add_u32 s76, s34, 0x2000
	s_addc_u32 s77, s35, 0
	s_add_i32 s75, s74, 0x14000
	s_mov_b32 m0, s75
	s_nop 0
	global_load_lds_dwordx4 v166, s[76:77]
	s_add_i32 s75, s74, 0x16000
	s_mov_b32 m0, s75
	s_nop 0
	global_load_lds_dwordx4 v167, s[76:77]
.Lmy_g9s4:
	s_and_b64 vcc, exec, s[18:19]
	s_cbranch_vccnz .Lmy_w9a0
	s_waitcnt vmcnt(6)

; #define PG8_STAGE(bufoff, gbase, voff) do { PG8_GLDS((const char*)(gbase), (voff)[0], ldsb + (bufoff)); PG8_GLDS((const char*)(gbase), (voff)[1], ldsb + (bufoff) + 8192u); } while (0)
; #define PG8_STAGEA(bufoff, gbase, o0, o1) do { PG8_GLDS((const char*)(gbase), (o0), ldsb + (bufoff)); PG8_GLDS((const char*)(gbase), (o1), ldsb + (bufoff) + 8192u); } while (0)
; #define PG8_STAGEA1(bufoff, gbase) do { if constexpr (Sched::GATHER) { PG8_STAGEA(bufoff, gbase, vA2, vA3); } else { PG8_STAGEA(bufoff, (gbase) + hstep, vA0, vA1); } } while (0)
; #define PG8_LDA(dst, b, h) do { if constexpr (F8) { _Pragma("unroll") for (int m = 0; m < 4; ++m) dst##8[m] = PG8_LD32(lds + PG8_SA(b, h) + aoff + m * 2048); } else { \
;         _Pragma("unroll") for (int m = 0; m < 4; ++m) _Pragma("unroll") for (int k = 0; k < 2; ++k) dst[m][k] = *(const LAS bf16x8*)(lds + PG8_SA(b, h) + aoff + m * 2048 + k * 1024); } } while (0)
; #define PG8_LDB(dst, b, h) do { if constexpr (F8) { _Pragma("unroll") for (int n = 0; n < 2; ++n) dst##8[n] = PG8_LD32(lds + PG8_SB(b, h) + boff + n * 2048); } else { \
;         _Pragma("unroll") for (int n = 0; n < 2; ++n) _Pragma("unroll") for (int k = 0; k < 2; ++k) dst[n][k] = *(const LAS bf16x8*)(lds + PG8_SB(b, h) + boff + n * 2048 + k * 1024); } } while (0)
; #define PG8_WAIT_VR() PG8_WAIT_V(8)
; #define PG8_WAIT_VX() do { if (relax) asm volatile("s_waitcnt vmcnt(%0)" :: "n"(8 + Epi::RELAX) : "memory"); else PG8_WAIT_V(8); } while (0)
; #define PG8_WAIT_L(n) asm volatile("s_waitcnt lgkmcnt(" #n ")" ::: "memory")
; #define PG8_BAR __builtin_amdgcn_s_barrier()
; template <class Epi, class Sched, bool F8 = false, bool PF = false, bool I8 = false, int PID = -1>
; __device__ __forceinline__ void gemm_phase(LAS unsigned char* lds, LAS unsigned char* xlds, const int RP, const int RPB, const int nt, const Sched& S, const Epi& E, const int stagger_ticks) {
;     ...
;             PG8_WAIT_VX(); PG8_WAIT_L(0); PG8_BAR; PG8_MMA(1, 0, At, B0); PG8_MMA(1, 1, At, B1); PG8_BAR; PG8_SCHED;
;             PG8_LDB(B0, 1, 0); PG8_LDB(B1, 1, 1); PG8_SCHED; PG8_LDA(At, 1, 0); PG8_STAGEA1(PG8_SA(0, 1), a2);
;             PG8_WAIT_VR(); PG8_WAIT_L(0); PG8_BAR; PG8_MMA(0, 0, At, B0); PG8_MMA(0, 1, At, B1); PG8_BAR; PG8_SCHED;
;             PG8_LDA(At, 1, 1); PG8_STAGE(PG8_SB(1, 0), b3, voffB); PG8_STAGE(PG8_SB(1, 1), b3 + hstepB, voffB); PG8_STAGEA(PG8_SA(1, 0), a3, vA0, vA1);
.Lmy_w9b0:
	s_barrier
	s_add_i32 s75, s74, 0x2000
	s_mov_b32 m0, s74
	s_nop 0
	global_load_lds_dwordx4 v164, s[38:39]
	s_nop 0
	s_mov_b32 m0, s75
	s_nop 0
	global_load_lds_dwordx4 v165, s[38:39]
	v_add_u32_e32 v14, 0x18000, v168
	v_add_u32_e32 v30, 0x1c000, v168
	ds_read_b128 v[2:5], v14
	ds_read_b128 v[6:9], v14 offset:1024
	ds_read_b128 v[10:13], v14 offset:2048
	ds_read_b128 v[14:17], v14 offset:3072
	ds_read_b128 v[18:21], v30
	ds_read_b128 v[22:25], v30 offset:1024
	ds_read_b128 v[26:29], v30 offset:2048
	ds_read_b128 v[30:33], v30 offset:3072
	ds_read_b128 v[34:37], v169 offset:32768
	ds_read_b128 v[38:41], v169 offset:33792
	ds_read_b128 v[42:45], v169 offset:34816
	ds_read_b128 v[46:49], v169 offset:35840
	ds_read_b128 v[50:53], v169 offset:36864
	ds_read_b128 v[54:57], v169 offset:37888
	ds_read_b128 v[58:61], v169 offset:38912
	ds_read_b128 v[62:65], v169 offset:39936
	s_add_u32 s38, s38, 0x20000
	s_addc_u32 s39, s39, 0
	s_add_i32 s75, s74, 0x4000
	s_mov_b32 m0, s75
	s_nop 0
	global_load_lds_dwordx4 v164, s[38:39]
	s_add_i32 s75, s74, 0x6000
	s_mov_b32 m0, s75
	s_nop 0
	global_load_lds_dwordx4 v165, s[38:39]
	s_waitcnt vmcnt(8)
	s_waitcnt lgkmcnt(0)
	s_barrier
	s_setprio 1
	s_and_b64 vcc, exec, s[18:19]
	s_waitcnt lgkmcnt(6)
	v_mfma_f32_16x16x128_f8f6f4 v[150:153], v[2:9], v[34:41], v[150:153]
	v_mfma_f32_16x16x128_f8f6f4 v[146:149], v[10:17], v[34:41], v[146:149]
	s_cbranch_vccnz .Lmy_g9x5
	s_add_i32 s98, s74, 0x18000
	s_mov_b32 m0, s98
	s_nop 0
	global_load_lds_dwordx4 v166, s[36:37]
.Lmy_g9x5:
	s_waitcnt lgkmcnt(4)
	v_mfma_f32_16x16x128_f8f6f4 v[134:137], v[2:9], v[42:49], v[134:137]
	v_mfma_f32_16x16x128_f8f6f4 v[130:133], v[10:17], v[42:49], v[130:133]
	s_cbranch_vccnz .Lmy_g9x6
	s_add_i32 s98, s74, 0x1a000
	s_mov_b32 m0, s98
	s_nop 0
	global_load_lds_dwordx4 v167, s[36:37]
.Lmy_g9x6:
	s_waitcnt lgkmcnt(2)
	v_mfma_f32_16x16x128_f8f6f4 v[118:121], v[2:9], v[50:57], v[118:121]
	v_mfma_f32_16x16x128_f8f6f4 v[114:117], v[10:17], v[50:57], v[114:117]
	s_cbranch_vccnz .Lmy_g9x7
	s_add_u32 s100, s34, 0x2080
	s_addc_u32 s101, s35, 0
	s_add_i32 s98, s74, 0x1c000
	s_mov_b32 m0, s98
	s_nop 0
	global_load_lds_dwordx4 v166, s[100:101]
.Lmy_g9x7:
	s_waitcnt lgkmcnt(0)
	v_mfma_f32_16x16x128_f8f6f4 v[102:105], v[2:9], v[58:65], v[102:105]
	v_mfma_f32_16x16x128_f8f6f4 v[98:101], v[10:17], v[58:65], v[98:101]
	s_cbranch_vccnz .Lmy_g9x8
	s_add_i32 s98, s74, 0x1e000
	s_mov_b32 m0, s98
	s_nop 0
	global_load_lds_dwordx4 v167, s[100:101]
.Lmy_g9x8:
	v_mfma_f32_16x16x128_f8f6f4 v[158:161], v[18:25], v[34:41], v[158:161]
	v_mfma_f32_16x16x128_f8f6f4 v[154:157], v[26:33], v[34:41], v[154:157]
	v_mfma_f32_16x16x128_f8f6f4 v[142:145], v[18:25], v[42:49], v[142:145]
	v_mfma_f32_16x16x128_f8f6f4 v[138:141], v[26:33], v[42:49], v[138:141]
	v_mfma_f32_16x16x128_f8f6f4 v[126:129], v[18:25], v[50:57], v[126:129]
	v_mfma_f32_16x16x128_f8f6f4 v[122:125], v[26:33], v[50:57], v[122:125]
	v_mfma_f32_16x16x128_f8f6f4 v[110:113], v[18:25], v[58:65], v[110:113]
	v_mfma_f32_16x16x128_f8f6f4 v[106:109], v[26:33], v[58:65], v[106:109]
	s_setprio 0
	s_barrier
	ds_read_b128 v[42:45], v169 offset:49152
	ds_read_b128 v[46:49], v169 offset:50176
	ds_read_b128 v[58:61], v169 offset:51200
	ds_read_b128 v[62:65], v169 offset:52224
	ds_read_b128 v[170:173], v169 offset:53248
	ds_read_b128 v[174:177], v169 offset:54272
	ds_read_b128 v[178:181], v169 offset:55296
	ds_read_b128 v[182:185], v169 offset:56320
	s_and_b64 vcc, exec, s[18:19]
	s_cbranch_vccz .Lmy_g9s9
	s_add_i32 s38, s74, 0x18000
	s_mov_b32 m0, s38
	s_nop 0
	global_load_lds_dwordx4 v166, s[36:37]
	s_add_i32 s38, s74, 0x1a000
	s_mov_b32 m0, s38
	s_nop 0
	global_load_lds_dwordx4 v167, s[36:37]
	s_add_u32 s34, s34, 0x2080
	s_addc_u32 s35, s35, 0
	s_add_i32 s36, s74, 0x1c000
	s_mov_b32 m0, s36
	s_nop 0
	global_load_lds_dwordx4 v166, s[34:35]
	s_add_i32 s36, s74, 0x1e000
	s_mov_b32 m0, s36
	s_nop 0
	global_load_lds_dwordx4 v167, s[34:35]

; #define PG8_STAGEA1(bufoff, gbase) do { if constexpr (Sched::GATHER) { PG8_STAGEA(bufoff, gbase, vA2, vA3); } else { PG8_STAGEA(bufoff, (gbase) + hstep, vA0, vA1); } } while (0)
; #define PG8_LDA(dst, b, h) do { if constexpr (F8) { _Pragma("unroll") for (int m = 0; m < 4; ++m) dst##8[m] = PG8_LD32(lds + PG8_SA(b, h) + aoff + m * 2048); } else { \
;         _Pragma("unroll") for (int m = 0; m < 4; ++m) _Pragma("unroll") for (int k = 0; k < 2; ++k) dst[m][k] = *(const LAS bf16x8*)(lds + PG8_SA(b, h) + aoff + m * 2048 + k * 1024); } } while (0)
; #define PG8_LDB(dst, b, h) do { if constexpr (F8) { _Pragma("unroll") for (int n = 0; n < 2; ++n) dst##8[n] = PG8_LD32(lds + PG8_SB(b, h) + boff + n * 2048); } else { \
;         _Pragma("unroll") for (int n = 0; n < 2; ++n) _Pragma("unroll") for (int k = 0; k < 2; ++k) dst[n][k] = *(const LAS bf16x8*)(lds + PG8_SB(b, h) + boff + n * 2048 + k * 1024); } } while (0)
; #define PG8_WAIT_VX() do { if (relax) asm volatile("s_waitcnt vmcnt(%0)" :: "n"(8 + Epi::RELAX) : "memory"); else PG8_WAIT_V(8); } while (0)
; #define PG8_WAIT_L(n) asm volatile("s_waitcnt lgkmcnt(" #n ")" ::: "memory")
; #define PG8_BAR __builtin_amdgcn_s_barrier()
; #define PG8_SCHED __builtin_amdgcn_sched_barrier(0)
; template <class Epi, class Sched, bool F8 = false, bool PF = false, bool I8 = false, int PID = -1>
; __device__ __forceinline__ void gemm_phase(LAS unsigned char* lds, LAS unsigned char* xlds, const int RP, const int RPB, const int nt, const Sched& S, const Epi& E, const int stagger_ticks) {
;     ...
;             PG8_LDB(B0, 0, 0); PG8_LDB(B1, 0, 1); PG8_SCHED; PG8_LDA(At, 0, 0); PG8_STAGEA1(PG8_SA(1, 1), a1);
;             if (Sched::GATHER) { if (last) { const u32x4 nv = *nslot; vA0 = nv.x; vA1 = nv.y; vA2 = nv.z; vA3 = nv.w; } }
;             PG8_WAIT_VX(); PG8_WAIT_L(0); PG8_BAR; PG8_MMA(0, 0, At, B0); PG8_MMA(0, 1, At, B1); PG8_BAR; PG8_SCHED;
.LBB0_1063:
	s_mov_b32 s74, s47
	s_add_u32 s100, s26, 0xfffe0000
	s_addc_u32 s101, s27, -1
	s_add_i32 s30, s74, 0x8000
	s_mov_b32 m0, s30
	s_nop 0
	global_load_lds_dwordx4 v164, s[100:101]
	s_add_i32 s30, s74, 0xa000
	s_mov_b32 m0, s30
	s_nop 0
	global_load_lds_dwordx4 v165, s[100:101]
	v_add_u32_e32 v14, 0x10000, v168
	v_add_u32_e32 v30, 0x14000, v168
	ds_read_b128 v[2:5], v14
	ds_read_b128 v[6:9], v14 offset:1024
	ds_read_b128 v[10:13], v14 offset:2048
	ds_read_b128 v[14:17], v14 offset:3072
	ds_read_b128 v[18:21], v30
	ds_read_b128 v[22:25], v30 offset:1024
	ds_read_b128 v[26:29], v30 offset:2048
	ds_read_b128 v[30:33], v30 offset:3072
	ds_read_b128 v[170:173], v169
	ds_read_b128 v[174:177], v169 offset:1024
	ds_read_b128 v[178:181], v169 offset:2048
	ds_read_b128 v[182:185], v169 offset:3072
	ds_read_b128 v[186:189], v169 offset:4096
	ds_read_b128 v[190:193], v169 offset:5120
	ds_read_b128 v[194:197], v169 offset:6144
	ds_read_b128 v[198:201], v169 offset:7168
	s_add_i32 s30, s74, 0xc000
	s_mov_b32 m0, s30
	s_nop 0
	global_load_lds_dwordx4 v164, s[26:27]
	s_add_i32 s30, s74, 0xe000
	s_mov_b32 m0, s30
	s_nop 0
	global_load_lds_dwordx4 v165, s[26:27]
	s_waitcnt vmcnt(8)
	s_waitcnt lgkmcnt(0)
	s_barrier
	s_setprio 1
	s_cmp_eq_u32 s73, 4
	s_cselect_b32 s100, s8, s25
	s_cselect_b32 s101, s9, s71
	s_and_b64 vcc, exec, s[18:19]
	s_waitcnt lgkmcnt(6)
	v_mfma_f32_16x16x128_f8f6f4 v[150:153], v[2:9], v[170:177], v[150:153]
	v_mfma_f32_16x16x128_f8f6f4 v[146:149], v[10:17], v[170:177], v[146:149]
	s_cbranch_vccnz .Lmy_g9x0
	s_add_i32 s98, s74, 0x10000
	s_mov_b32 m0, s98
	s_nop 0
	global_load_lds_dwordx4 v166, s[100:101]
.Lmy_g9x0:
	s_waitcnt lgkmcnt(4)
	v_mfma_f32_16x16x128_f8f6f4 v[134:137], v[2:9], v[178:185], v[134:137]
	v_mfma_f32_16x16x128_f8f6f4 v[130:133], v[10:17], v[178:185], v[130:133]
	s_cbranch_vccnz .Lmy_g9x1
	s_add_i32 s98, s74, 0x12000
	s_mov_b32 m0, s98
	s_nop 0
	global_load_lds_dwordx4 v167, s[100:101]
.Lmy_g9x1:
	s_waitcnt lgkmcnt(2)
	v_mfma_f32_16x16x128_f8f6f4 v[118:121], v[2:9], v[186:193], v[118:121]
	v_mfma_f32_16x16x128_f8f6f4 v[114:117], v[10:17], v[186:193], v[114:117]
	s_cbranch_vccnz .Lmy_g9x2
	s_add_u32 s100, s100, 0x2000
	s_addc_u32 s101, s101, 0
	s_add_i32 s98, s74, 0x14000
	s_mov_b32 m0, s98
	s_nop 0
	global_load_lds_dwordx4 v166, s[100:101]
.Lmy_g9x2:
	s_waitcnt lgkmcnt(0)
	v_mfma_f32_16x16x128_f8f6f4 v[102:105], v[2:9], v[194:201], v[102:105]
	v_mfma_f32_16x16x128_f8f6f4 v[98:101], v[10:17], v[194:201], v[98:101]
	s_cbranch_vccnz .Lmy_g9x3
	s_add_i32 s98, s74, 0x16000
	s_mov_b32 m0, s98
	s_nop 0
	global_load_lds_dwordx4 v167, s[100:101]
.Lmy_g9x3:
	v_mfma_f32_16x16x128_f8f6f4 v[158:161], v[18:25], v[170:177], v[158:161]
	v_mfma_f32_16x16x128_f8f6f4 v[154:157], v[26:33], v[170:177], v[154:157]
	v_mfma_f32_16x16x128_f8f6f4 v[142:145], v[18:25], v[178:185], v[142:145]
	v_mfma_f32_16x16x128_f8f6f4 v[138:141], v[26:33], v[178:185], v[138:141]
	v_mfma_f32_16x16x128_f8f6f4 v[126:129], v[18:25], v[186:193], v[126:129]
	v_mfma_f32_16x16x128_f8f6f4 v[122:125], v[26:33], v[186:193], v[122:125]
	v_mfma_f32_16x16x128_f8f6f4 v[110:113], v[18:25], v[194:201], v[110:113]
	v_mfma_f32_16x16x128_f8f6f4 v[106:109], v[26:33], v[194:201], v[106:109]
	s_setprio 0
	s_barrier
	s_cmp_lg_u32 s73, -2
	s_cselect_b64 s[30:31], -1, 0
	s_or_b64 s[30:31], s[30:31], s[28:29]
	s_and_b64 vcc, exec, s[30:31]
	s_cbranch_vccnz .LBB0_1062
	s_mov_b32 m0, s72
	s_nop 0
	global_load_lds_dword v1, s[2:3]
	s_branch .LBB0_1062
.Lmy_z8t:
	s_mov_b32 s74, s47
	s_add_u32 s100, s26, 0xfffe0000
	s_addc_u32 s101, s27, -1
	s_add_i32 s30, s74, 0x8000
	s_mov_b32 m0, s30
	s_nop 0
	global_load_lds_dwordx4 v164, s[100:101]
	s_add_i32 s30, s74, 0xa000
	s_mov_b32 m0, s30
	s_nop 0
	global_load_lds_dwordx4 v165, s[100:101]
	v_add_u32_e32 v14, 0x10000, v168
	v_add_u32_e32 v30, 0x14000, v168
	ds_read_b128 v[2:5], v14
	ds_read_b128 v[6:9], v14 offset:1024
	ds_read_b128 v[10:13], v14 offset:2048
	ds_read_b128 v[14:17], v14 offset:3072
	ds_read_b128 v[18:21], v30
	ds_read_b128 v[22:25], v30 offset:1024
	ds_read_b128 v[26:29], v30 offset:2048
	ds_read_b128 v[30:33], v30 offset:3072
	ds_read_b128 v[170:173], v169
	ds_read_b128 v[174:177], v169 offset:1024
	ds_read_b128 v[178:181], v169 offset:2048
	ds_read_b128 v[182:185], v169 offset:3072
	ds_read_b128 v[186:189], v169 offset:4096
	ds_read_b128 v[190:193], v169 offset:5120
	ds_read_b128 v[194:197], v169 offset:6144
	ds_read_b128 v[198:201], v169 offset:7168
	s_add_i32 s30, s74, 0xc000
	s_mov_b32 m0, s30
	s_nop 0
	global_load_lds_dwordx4 v164, s[26:27]
	s_add_i32 s30, s74, 0xe000
	s_mov_b32 m0, s30
	s_nop 0
	global_load_lds_dwordx4 v165, s[26:27]
	s_waitcnt vmcnt(8)
	s_waitcnt lgkmcnt(0)
	s_barrier
	s_setprio 1
	s_cmp_eq_u32 s73, 4
	s_cselect_b32 s100, s8, s25
	s_cselect_b32 s101, s9, s71
	s_and_b64 vcc, exec, s[18:19]
	s_waitcnt lgkmcnt(6)
	v_mfma_f32_16x16x128_f8f6f4 v[150:153], v[2:9], v[170:177], 0
	v_mfma_f32_16x16x128_f8f6f4 v[146:149], v[10:17], v[170:177], 0
	s_cbranch_vccnz .Lmy_g9x10
	s_add_i32 s98, s74, 0x10000
	s_mov_b32 m0, s98
	s_nop 0
	global_load_lds_dwordx4 v166, s[100:101]
.Lmy_g9x10:
	s_waitcnt lgkmcnt(4)
	v_mfma_f32_16x16x128_f8f6f4 v[134:137], v[2:9], v[178:185], 0
	v_mfma_f32_16x16x128_f8f6f4 v[130:133], v[10:17], v[178:185], 0
	s_cbranch_vccnz .Lmy_g9x11
	s_add_i32 s98, s74, 0x12000
	s_mov_b32 m0, s98
	s_nop 0
	global_load_lds_dwordx4 v167, s[100:101]
.Lmy_g9x11:
	s_waitcnt lgkmcnt(2)
	v_mfma_f32_16x16x128_f8f6f4 v[118:121], v[2:9], v[186:193], 0
	v_mfma_f32_16x16x128_f8f6f4 v[114:117], v[10:17], v[186:193], 0
	s_cbranch_vccnz .Lmy_g9x12
	s_add_u32 s100, s100, 0x2000
	s_addc_u32 s101, s101, 0
	s_add_i32 s98, s74, 0x14000
	s_mov_b32 m0, s98
	s_nop 0
	global_load_lds_dwordx4 v166, s[100:101]
.Lmy_g9x12:
	s_waitcnt lgkmcnt(0)
	v_mfma_f32_16x16x128_f8f6f4 v[102:105], v[2:9], v[194:201], 0
	v_mfma_f32_16x16x128_f8f6f4 v[98:101], v[10:17], v[194:201], 0
	s_cbranch_vccnz .Lmy_g9x13
	s_add_i32 s98, s74, 0x16000
	s_mov_b32 m0, s98
	s_nop 0
	global_load_lds_dwordx4 v167, s[100:101]
.Lmy_g9x13:
	v_mfma_f32_16x16x128_f8f6f4 v[158:161], v[18:25], v[170:177], 0
	v_mfma_f32_16x16x128_f8f6f4 v[154:157], v[26:33], v[170:177], 0
	v_mfma_f32_16x16x128_f8f6f4 v[142:145], v[18:25], v[178:185], 0
	v_mfma_f32_16x16x128_f8f6f4 v[138:141], v[26:33], v[178:185], 0
	v_mfma_f32_16x16x128_f8f6f4 v[126:129], v[18:25], v[186:193], 0
	v_mfma_f32_16x16x128_f8f6f4 v[122:125], v[26:33], v[186:193], 0
	v_mfma_f32_16x16x128_f8f6f4 v[110:113], v[18:25], v[194:201], 0
	v_mfma_f32_16x16x128_f8f6f4 v[106:109], v[26:33], v[194:201], 0
	s_setprio 0
	s_barrier
	s_cmp_lg_u32 s73, -2
	s_cselect_b64 s[30:31], -1, 0
	s_or_b64 s[30:31], s[30:31], s[28:29]
	s_and_b64 vcc, exec, s[30:31]
	s_cbranch_vccnz .Lmy_z8b
	s_mov_b32 m0, s72
	s_nop 0
	global_load_lds_dword v1, s[2:3]
	s_branch .Lmy_z8b
